# diff softmax segment second trim (rare-path scalars, dead branch logic, nop fillers) on top of v033
# speedup vs baseline: 1.0458x; 1.0011x over previous
; #define PK4(P, BASE, OUT) do { u32x4 w = {cvtpk(P[BASE + 0], P[BASE + 1]), cvtpk(P[BASE + 2], P[BASE + 3]), cvtpk(P[BASE + 4], P[BASE + 5]), cvtpk(P[BASE + 6], P[BASE + 7])}; \
;     OUT = *reinterpret_cast<bf16x8*>(&w); } while (0)
; __device__ __forceinline__ void smax_tile(f32x16& p0, f32x16& p1, float& mhat, float& l_reg, f32x16 (&o)[4], float* al_l, const bool first, int r32, int hi,
;                                           bf16x8& pa0, bf16x8& pa1, bf16x8& pa2, bf16x8& pa3) {
;     ...
; #pragma unroll
;     for (int r = 0; r < 16; ++r) p0[r] = __builtin_amdgcn_exp2f(p0[r]);
; #pragma unroll
;     for (int r = 0; r < 16; ++r) p1[r] = __builtin_amdgcn_exp2f(p1[r]);
;     float ps = p0[0];
; #pragma unroll
;     for (int r = 1; r < 16; ++r) ps += p0[r];
; #pragma unroll
;     for (int r = 0; r < 16; ++r) ps += p1[r];
;     { auto rr = __builtin_amdgcn_permlane32_swap(__float_as_uint(ps), __float_as_uint(ps), false, false); ps = __uint_as_float(rr[0]) + __uint_as_float(rr[1]); }
;     l_reg += ps;
;     ...
;     PK4(p0, 0, pa0); PK4(p0, 8, pa1); PK4(p1, 0, pa2); PK4(p1, 8, pa3);
.LBB0_651:
	v_exp_f32_e32 v96, v96
	v_exp_f32_e32 v97, v97
	v_exp_f32_e32 v98, v98
	v_exp_f32_e32 v99, v99
	v_exp_f32_e32 v100, v100
	v_exp_f32_e32 v101, v101
	v_add_f32_e32 v128, v96, v97
	v_exp_f32_e32 v102, v102
	v_add_f32_e32 v128, v98, v128
	v_exp_f32_e32 v103, v103
	v_add_f32_e32 v128, v99, v128
	v_exp_f32_e32 v104, v104
	v_add_f32_e32 v128, v100, v128
	v_exp_f32_e32 v105, v105
	v_add_f32_e32 v128, v101, v128
	v_exp_f32_e32 v106, v106
	v_add_f32_e32 v128, v102, v128
	v_exp_f32_e32 v107, v107
	v_add_f32_e32 v128, v103, v128
	v_exp_f32_e32 v108, v108
	v_add_f32_e32 v128, v104, v128
	v_exp_f32_e32 v109, v109
	v_add_f32_e32 v128, v105, v128
	v_exp_f32_e32 v110, v110
	v_add_f32_e32 v128, v106, v128
	v_exp_f32_e32 v111, v111
	v_add_f32_e32 v128, v107, v128
	v_exp_f32_e32 v80, v80
	v_add_f32_e32 v128, v108, v128
	v_exp_f32_e32 v81, v81
	v_add_f32_e32 v128, v109, v128
	v_exp_f32_e32 v82, v82
	v_add_f32_e32 v128, v110, v128
	v_exp_f32_e32 v83, v83
	v_add_f32_e32 v128, v111, v128
	v_exp_f32_e32 v84, v84
	v_add_f32_e32 v128, v80, v128
	v_exp_f32_e32 v85, v85
	v_add_f32_e32 v128, v81, v128
	v_exp_f32_e32 v86, v86
	v_add_f32_e32 v128, v82, v128
	v_exp_f32_e32 v87, v87
	v_add_f32_e32 v128, v83, v128
	v_exp_f32_e32 v88, v88
	v_add_f32_e32 v128, v84, v128
	v_exp_f32_e32 v89, v89
	v_add_f32_e32 v128, v85, v128
	v_exp_f32_e32 v90, v90
	v_add_f32_e32 v128, v86, v128
	v_exp_f32_e32 v91, v91
	v_add_f32_e32 v128, v87, v128
	v_exp_f32_e32 v92, v92
	v_add_f32_e32 v128, v88, v128
	v_exp_f32_e32 v93, v93
	v_add_f32_e32 v128, v89, v128
	v_exp_f32_e32 v94, v94
	v_add_f32_e32 v128, v90, v128
	v_exp_f32_e32 v95, v95
	v_add_f32_e32 v128, v91, v128
	v_add_f32_e32 v128, v92, v128
	v_add_f32_e32 v128, v93, v128
	v_add_f32_e32 v128, v94, v128
	v_add_f32_e32 v128, v95, v128
	v_mov_b32_e32 v129, v128
	v_cvt_pk_bf16_f32 v162, v96, v97
	v_cvt_pk_bf16_f32 v163, v98, v99
	v_permlane32_swap_b32_e32 v128, v129
	v_add_f32_e32 v128, v128, v129
	v_add_f32_e32 v159, v159, v128
	v_cvt_pk_bf16_f32 v164, v100, v101
	v_cvt_pk_bf16_f32 v165, v102, v103
	v_cvt_pk_bf16_f32 v166, v104, v105
	v_cvt_pk_bf16_f32 v167, v106, v107
	v_cvt_pk_bf16_f32 v168, v108, v109
	v_cvt_pk_bf16_f32 v169, v110, v111
	v_cvt_pk_bf16_f32 v132, v80, v81
	v_cvt_pk_bf16_f32 v133, v82, v83
	v_cvt_pk_bf16_f32 v134, v84, v85
	v_cvt_pk_bf16_f32 v135, v86, v87
	v_cvt_pk_bf16_f32 v128, v88, v89
	v_cvt_pk_bf16_f32 v129, v90, v91
	v_cvt_pk_bf16_f32 v130, v92, v93
	v_cvt_pk_bf16_f32 v131, v94, v95
	s_cmp_lg_u32 s86, 0
	s_waitcnt lgkmcnt(0)
	s_barrier
; template <int DQK, bool HASQK, bool HASPV, int J>
; __device__ __forceinline__ void slot_read(bf16x8 (&kf)[DQK / 16][2], s16x4 (&vf)[4][8], const int (&ka_)[4], int vb_) {
;     constexpr int NQS = HASQK ? 2 * (DQK / 16) : 0, NS = NQS + (HASPV ? 16 : 0);
;     if constexpr (J < NQS) { constexpr int d0 = J >> 1, h = J & 1; dsr128<(d0 >> 2) * 128 + h * 32 * DQK * 2>(kf[d0][h], ka_[d0 & 3]); }
;     else if constexpr (J < NS) { constexpr int q = J - NQS, g = q >> 2, d = q & 3; dstr64<v_rd_off(d, g, 0)>(vf[g][2 * d], vb_); dstr64<v_rd_off(d, g, 1)>(vf[g][2 * d + 1], vb_); }
; }
; template <int DQK, bool HASQK, bool HASPV, int J> ...
;     constexpr int NQS = HASQK ? 2 * (DQK / 16) : 0, NS = NQS + (HASPV ? 16 : 0);
;     if constexpr (J < NS) {
;         constexpr int rd1 = (J + 1 < NS) ? ((J + 1 < NQS) ? 1 : 2) : 0, rd2 = (J + 2 < NS) ? ((J + 2 < NQS) ? 1 : 2) : 0, rd3 = (J + 3 < NS) ? ((J + 3 < NQS) ? 1 : 2) : 0, NW = rd1 + rd2 + rd3;
;     ...
;         if constexpr (J < NQS) { constexpr int d0 = J >> 1, h = J & 1;
;             LWN1(kf[d0][h]); SBAR();
;             if constexpr (h == 0) p0 = __builtin_amdgcn_mfma_f32_32x32x16_bf16(kf[d0][0], qr[d0], (d0 == 0) ? negm : p0, 0, 0, 0);
;             else p1 = __builtin_amdgcn_mfma_f32_32x32x16_bf16(kf[d0][1], qr[d0], (d0 == 0) ? negm : p1, 0, 0, 0);
;         } else { constexpr int q = J - NQS, g = q >> 2, d = q & 3;
;             LWN2(vf[g][2 * d], vf[g][2 * d + 1]); SBAR();
;             o[d] = __builtin_amdgcn_mfma_f32_32x32x16_bf16(pa[g], (bf16x8){vf[g][2 * d][0], vf[g][2 * d][1], vf[g][2 * d][2], vf[g][2 * d][3], vf[g][2 * d + 1][0], vf[g][2 * d + 1][1], vf[g][2 * d + 1][2], vf[g][2 * d + 1][3]}, o[d], 0, 0, 0);
;         }
;     ...
;         SBAR();
;         slot_read<DQK, HASQK, HASPV, J + 4>(kf, vf, ka_, vb_);
;         SBAR();
;         slot_run<DQK, HASQK, HASPV, J + 1>(kf, vf, ka_, vb_, qr, p0, p1, negm, o, pa);
;     }
; }
;     ...
;     for (int i = 0; i < NT - 1; ++i) {
;         SEG_S(i);
;         { const int cp = (ci == 0) ? 2 : ci - 1, cn = (ci == 2) ? 0 : ci + 1;
;           if (DMA_M) { if (i + 3 < NT) DMA_K(i + 3, cp); if (i + 2 < NT) DMA_V(i + 2, cn); }
;           SEG_M(true, true, ci, cp);
;           if (DMA_M && i + 3 < NT) asm volatile("s_waitcnt vmcnt(%0)" :: "n"(NKW + 2) : "memory");
;           else asm volatile("s_waitcnt vmcnt(0)" ::: "memory");
;           BAR_ALL(); }
	s_cselect_b32 s46, s87, 0x8000
	s_lshl_b32 s47, s86, 13
	v_add_u32_e32 v81, s47, v141
	v_add_u32_e32 v82, s47, v143
	ds_read_b128 v[170:173], v81 offset:0
	ds_read_b128 v[174:177], v81 offset:0x1000
	ds_read_b128 v[178:181], v82 offset:0
	ds_read_b128 v[182:185], v82 offset:0x1000
	v_xor_b32_e32 v80, 0x80000000, v158
	v_add_u32_e32 v186, s47, v160
	v_add_u32_e32 v187, s47, v161
	v_add_u32_e32 v188, s46, v157
	v_mov_b32_e32 v81, v80
	v_mov_b32_e32 v82, v80
	v_mov_b32_e32 v83, v80
	v_mov_b32_e32 v84, v80
	v_mov_b32_e32 v85, v80
	v_mov_b32_e32 v86, v80
	v_mov_b32_e32 v87, v80
	v_mov_b32_e32 v88, v80
	v_mov_b32_e32 v89, v80
	v_mov_b32_e32 v90, v80
	v_mov_b32_e32 v91, v80
	v_mov_b32_e32 v92, v80
	v_mov_b32_e32 v93, v80
	v_mov_b32_e32 v94, v80
	v_mov_b32_e32 v95, v80
	s_waitcnt lgkmcnt(3)
	s_nop 1
	v_mfma_f32_32x32x16_bf16 v[96:111], v[170:173], v[112:115], v[80:95]
	ds_read_b128 v[170:173], v186 offset:0
	s_waitcnt lgkmcnt(3)
	s_nop 0
	v_mfma_f32_32x32x16_bf16 v[80:95], v[174:177], v[112:115], v[80:95]
	ds_read_b128 v[174:177], v186 offset:0x1000
	s_waitcnt lgkmcnt(3)
	s_nop 0
	v_mfma_f32_32x32x16_bf16 v[96:111], v[178:181], v[116:119], v[96:111]
	ds_read_b128 v[178:181], v187 offset:0
	s_waitcnt lgkmcnt(3)
	s_nop 0
	v_mfma_f32_32x32x16_bf16 v[80:95], v[182:185], v[116:119], v[80:95]
	ds_read_b128 v[182:185], v187 offset:0x1000
	s_waitcnt lgkmcnt(3)
	s_nop 0
	v_mfma_f32_32x32x16_bf16 v[96:111], v[170:173], v[120:123], v[96:111]
	ds_read_b64_tr_b16 v[170:171], v188 offset:0
	ds_read_b64_tr_b16 v[172:173], v188 offset:0x800
	s_waitcnt lgkmcnt(4)
	s_nop 0
	v_mfma_f32_32x32x16_bf16 v[80:95], v[174:177], v[120:123], v[80:95]
	ds_read_b64_tr_b16 v[174:175], v188 offset:0x200
	ds_read_b64_tr_b16 v[176:177], v188 offset:0xa00
	s_waitcnt lgkmcnt(5)
	s_nop 0
	v_mfma_f32_32x32x16_bf16 v[96:111], v[178:181], v[124:127], v[96:111]
	ds_read_b64_tr_b16 v[178:179], v188 offset:0x400
	ds_read_b64_tr_b16 v[180:181], v188 offset:0xc00
	s_waitcnt lgkmcnt(6)
	s_nop 0
	v_mfma_f32_32x32x16_bf16 v[80:95], v[182:185], v[124:127], v[80:95]
	ds_read_b64_tr_b16 v[182:183], v188 offset:0x600
	ds_read_b64_tr_b16 v[184:185], v188 offset:0xe00
	s_waitcnt lgkmcnt(6)
	s_nop 0
	v_mfma_f32_32x32x16_bf16 v[64:79], v[162:165], v[170:173], v[64:79]
	ds_read_b64_tr_b16 v[170:171], v188 offset:0x1000
	ds_read_b64_tr_b16 v[172:173], v188 offset:0x1800
	s_waitcnt lgkmcnt(6)
	s_nop 0
	v_mfma_f32_32x32x16_bf16 v[48:63], v[162:165], v[174:177], v[48:63]
	ds_read_b64_tr_b16 v[174:175], v188 offset:0x1200
	ds_read_b64_tr_b16 v[176:177], v188 offset:0x1a00
	s_waitcnt lgkmcnt(6)
	s_nop 0
	v_mfma_f32_32x32x16_bf16 v[32:47], v[162:165], v[178:181], v[32:47]
	ds_read_b64_tr_b16 v[178:179], v188 offset:0x1400
	ds_read_b64_tr_b16 v[180:181], v188 offset:0x1c00
	s_waitcnt lgkmcnt(6)
	s_nop 0
	v_mfma_f32_32x32x16_bf16 v[16:31], v[162:165], v[182:185], v[16:31]
	ds_read_b64_tr_b16 v[162:163], v188 offset:0x1600
	ds_read_b64_tr_b16 v[164:165], v188 offset:0x1e00
	s_waitcnt lgkmcnt(6)
	s_nop 0
	v_mfma_f32_32x32x16_bf16 v[64:79], v[166:169], v[170:173], v[64:79]
	ds_read_b64_tr_b16 v[170:171], v188 offset:0x2000
	ds_read_b64_tr_b16 v[172:173], v188 offset:0x2800
	s_waitcnt lgkmcnt(6)
	s_nop 0
	v_mfma_f32_32x32x16_bf16 v[48:63], v[166:169], v[174:177], v[48:63]
	ds_read_b64_tr_b16 v[174:175], v188 offset:0x2200
	ds_read_b64_tr_b16 v[176:177], v188 offset:0x2a00
	s_waitcnt lgkmcnt(6)
	s_nop 0
	v_mfma_f32_32x32x16_bf16 v[32:47], v[166:169], v[178:181], v[32:47]
	ds_read_b64_tr_b16 v[178:179], v188 offset:0x2400
	ds_read_b64_tr_b16 v[180:181], v188 offset:0x2c00
	s_waitcnt lgkmcnt(6)
	s_nop 0
	v_mfma_f32_32x32x16_bf16 v[16:31], v[166:169], v[162:165], v[16:31]
	ds_read_b64_tr_b16 v[162:163], v188 offset:0x2600
	ds_read_b64_tr_b16 v[164:165], v188 offset:0x2e00
	s_waitcnt lgkmcnt(6)
	s_nop 0
	v_mfma_f32_32x32x16_bf16 v[64:79], v[132:135], v[170:173], v[64:79]
	ds_read_b64_tr_b16 v[166:167], v188 offset:0x3000
	ds_read_b64_tr_b16 v[168:169], v188 offset:0x3800
	s_waitcnt lgkmcnt(6)
	s_nop 0
	v_mfma_f32_32x32x16_bf16 v[48:63], v[132:135], v[174:177], v[48:63]
	ds_read_b64_tr_b16 v[170:171], v188 offset:0x3200
	ds_read_b64_tr_b16 v[172:173], v188 offset:0x3a00
	s_waitcnt lgkmcnt(6)
	s_nop 0
	v_mfma_f32_32x32x16_bf16 v[32:47], v[132:135], v[178:181], v[32:47]
	ds_read_b64_tr_b16 v[174:175], v188 offset:0x3400
	ds_read_b64_tr_b16 v[176:177], v188 offset:0x3c00
	s_waitcnt lgkmcnt(6)
	s_nop 0
	v_mfma_f32_32x32x16_bf16 v[16:31], v[132:135], v[162:165], v[16:31]
	ds_read_b64_tr_b16 v[132:133], v188 offset:0x3600
	ds_read_b64_tr_b16 v[134:135], v188 offset:0x3e00
	s_waitcnt lgkmcnt(6)
	s_nop 0
	v_mfma_f32_32x32x16_bf16 v[64:79], v[128:131], v[166:169], v[64:79]
	s_waitcnt lgkmcnt(4)
	s_nop 0
	v_mfma_f32_32x32x16_bf16 v[48:63], v[128:131], v[170:173], v[48:63]
	s_waitcnt lgkmcnt(2)
	s_nop 0
	v_mfma_f32_32x32x16_bf16 v[32:47], v[128:131], v[174:177], v[32:47]
	s_waitcnt lgkmcnt(0)
	s_nop 0
	v_mfma_f32_32x32x16_bf16 v[16:31], v[128:131], v[132:135], v[16:31]
	v_lshl_add_u64 v[144:145], v[144:145], 0, s[28:29]
	v_lshl_add_u64 v[146:147], v[146:147], 0, s[28:29]
	v_lshl_add_u64 v[148:149], v[148:149], 0, s[28:29]
	s_waitcnt vmcnt(0)
	s_add_u32 s44, s44, 0x10000
	s_waitcnt lgkmcnt(0)
	s_barrier
	s_addc_u32 s45, s45, 0
	s_cmp_eq_u32 s44, 0x7f0000
	s_cbranch_scc1 .LBB0_662

; __device__ __forceinline__ int crow(int r, int hi) { return (r & 3) + 8 * (r >> 2) + 4 * hi; }
; __device__ __forceinline__ float vmax3(float x, float y, float z) { float r; asm("v_max3_f32 %0, %1, %2, %3" : "=v"(r) : "v"(x), "v"(y), "v"(z)); return r; }
; __device__ __forceinline__ float vmax2(float x, float y) { float r; asm("v_max_f32 %0, %1, %2" : "=v"(r) : "v"(x), "v"(y)); return r; }
; __device__ __forceinline__ void smax_tile(f32x16& p0, f32x16& p1, float& mhat, float& l_reg, f32x16 (&o)[4], float* al_l, const bool first, int r32, int hi,
;                                           bf16x8& pa0, bf16x8& pa1, bf16x8& pa2, bf16x8& pa3) {
;     float a = vmax3(p0[0], p0[1], p1[0]), b = vmax3(p0[2], p0[3], p1[1]); a = vmax3(a, p1[2], p1[3]);
; #pragma unroll
;     for (int r = 4; r < 16; r += 4) { a = vmax3(a, p0[r], p0[r + 1]); b = vmax3(b, p0[r + 2], p0[r + 3]); a = vmax3(a, p1[r], p1[r + 1]); b = vmax3(b, p1[r + 2], p1[r + 3]); }
;     float rm = vmax2(a, b);
;     { auto rr = __builtin_amdgcn_permlane32_swap(__float_as_uint(rm), __float_as_uint(rm), false, false); rm = vmax2(__uint_as_float(rr[0]), __uint_as_float(rr[1])); }
;     if (__builtin_expect(first || __any(rm > THRL), 0)) {
;         const float dl = first ? rm : fmaxf(rm, 0.f);
;         mhat += dl;
; #pragma unroll
;         for (int r = 0; r < 16; ++r) { p0[r] -= dl; p1[r] -= dl; }
;         if (!first) { const float f = __builtin_amdgcn_exp2f(-dl); l_reg *= f;
;             if (hi == 0) al_l[r32] = f; asm volatile("s_waitcnt lgkmcnt(0)" ::: "memory");
; #pragma unroll
;             for (int d = 0; d < 4; ++d)
; #pragma unroll
;                 for (int r = 0; r < 16; ++r) o[d][r] *= al_l[crow(r, hi)]; }
;     }
.LBB0_654:
	s_add_i32 s46, s86, 1
	s_cmp_lg_u32 s86, 2
	s_cselect_b32 s86, s46, 0
	s_lshl_b32 s87, s86, 14
	s_add_i32 s46, s68, s87
	s_add_i32 m0, s46, 0x6000
	v_max3_f32 v128, v96, v97, v80
	global_load_lds_dwordx4 v[146:147], off
	s_add_i32 m0, s46, 0x6400
	v_max3_f32 v129, v98, v99, v81
	global_load_lds_dwordx4 v[148:149], off
	v_max3_f32 v128, v128, v82, v83
	v_max3_f32 v129, v129, v102, v103
	v_max3_f32 v128, v128, v100, v101
	v_max3_f32 v129, v129, v86, v87
	v_max3_f32 v128, v128, v84, v85
	v_max3_f32 v129, v129, v106, v107
	v_max3_f32 v128, v128, v104, v105
	v_max3_f32 v129, v129, v90, v91
	v_max3_f32 v128, v128, v88, v89
	v_max3_f32 v129, v129, v110, v111
	v_max3_f32 v128, v128, v108, v109
	v_max3_f32 v129, v129, v94, v95
	v_max3_f32 v128, v128, v92, v93
	v_max_f32 v128, v128, v129
	v_mov_b32_e32 v129, v128
	s_addk_i32 s87, 0xc000
	s_cmp_eq_u32 s44, 0
	v_permlane32_swap_b32_e32 v128, v129
	v_max_f32 v128, v128, v129
	s_cbranch_scc1 .LBB0_661
	v_cmp_lt_f32_e32 vcc, s79, v128
	s_cbranch_vccz .LBB0_651
	s_branch .LBB0_660
.LBB0_657:
	s_cmp_lg_u32 s44, 0
	s_cselect_b64 s[46:47], -1, 0
	s_andn2_b64 vcc, exec, s[46:47]
	s_cbranch_vccnz .LBB0_650
	v_exp_f32_e64 v129, -v128
	s_and_saveexec_b64 s[46:47], s[10:11]
	s_cbranch_execz .LBB0_649
	ds_write_b32 v155, v129 offset:128
	s_branch .LBB0_649
